# seam-wait hosting at seams 4-7 with the hosted waves delayed ~3 us (s_sleep) so the XCD leader's L2 writeback gets HBM first
# baseline (speedup 1.0000x reference)
; __device__ __forceinline__ unsigned xb_ld(unsigned* p)              { return __hip_atomic_load(p, __ATOMIC_RELAXED, __HIP_MEMORY_SCOPE_AGENT); }
; __device__ __forceinline__ unsigned xb_add(unsigned* p, unsigned v) { return __hip_atomic_fetch_add(p, v, __ATOMIC_RELAXED, __HIP_MEMORY_SCOPE_AGENT); }
; #define XB_SPIN(cond, bar) do { unsigned _sp = 0; while (cond) { __builtin_amdgcn_s_sleep(1); \
;     if ((++_sp & 255u) == 0u) { if (xb_ld(&(bar)[XB_TMO])) break; if (_sp > XB_SPIN_CAP) { atomicAdd(&(bar)[XB_TMO], 1u); break; } } } } while (0)
; #define SEAM(k) do { if (IN(k) && IN((k) + 1)) xcd_barrier(bar); } while (0)
; __device__ __forceinline__ void xcd_barrier(const XcdBarrier& b) {
;     asm volatile("s_waitcnt vmcnt(0)" ::: "memory");
;     __syncthreads();
;     if (threadIdx.x == 0) {
;         unsigned* bar = b.bar;
;         __builtin_amdgcn_s_waitcnt(0);
;         unsigned nloc = b.st[0], nx = b.st[1];
;         if (nloc == 0u) { xcd_barrier_complete(bar, b.x, nloc, nx); b.st[0] = nloc; b.st[1] = nx; }
;         const unsigned old = xb_add(&bar[XB_XSUB(b.x)], 1u);
;         const unsigned gen = old / nloc;
;         if (old + 1u == (gen + 1u) * nloc) {
;             __builtin_amdgcn_fence(__ATOMIC_RELEASE, "agent");
;             asm volatile("s_waitcnt vmcnt(0)" ::: "memory");
;             const unsigned og = xb_add(&bar[XB_TOP], 1u);
;             const unsigned tg = og / nx;
;             if (og + 1u == (tg + 1u) * nx) xb_add(&bar[XB_TOPGEN], 1u);
;             else XB_SPIN(xb_ld(&bar[XB_TOPGEN]) == tg, bar);
;             __builtin_amdgcn_fence(__ATOMIC_ACQUIRE, "agent");
;             xb_add(&bar[XB_XGEN(b.x)], 1u);
;             asm volatile("s_waitcnt vmcnt(0)" ::: "memory");
;         } else {
;             XB_SPIN(xb_ld(&bar[XB_XGEN(b.x)]) == gen, bar);
;             __builtin_amdgcn_fence(__ATOMIC_ACQUIRE, "agent");
;             asm volatile("s_waitcnt vmcnt(0)" ::: "memory");
;         }
;     }
;     __syncthreads();
; }
; __global__ void __launch_bounds__(NWAVES * 64, 2) mk_fwd(Args args) {
;     ...
;     SEAM(4);
;     if (IN(5)) {
;         pg8::Gemm g{(const bf16*)(ws + WS_MIX), (const bf16*)(ws + WS_WOUT), M, DM, DM, DM}; pg8::StaticOrder S; S.init(M, DM, G, bx);
;         pg8::EpiRes<1> E{nullptr, nullptr, HB, (float*)(ws + WS_SSQ1)};
;         STAGGER(1.5f); pg8::gemm_phase<pg8::EpiRes<1>, pg8::StaticOrder, true, true>(lds, g, S, E);
.LBB0_781:
	s_or_b64 exec, exec, s[4:5]
	s_cmp_lg_u32 s80, 0x100
	s_cbranch_scc1 .Lsh_skip_4
	s_cmp_lg_u32 s74, 0
	s_cbranch_scc1 .Lsh_skip_4
	s_cmp_lg_u32 s75, 12
	s_cbranch_scc1 .Lsh_skip_4
	v_readfirstlane_b32 s101, v0
	s_nop 3
	s_lshr_b32 s101, s101, 6
	s_cmp_eq_u32 s101, 0
	s_cbranch_scc1 .Lsh_skip_4
	s_sleep 100
	v_writelane_b32 v255, s0, 20
	v_writelane_b32 v255, s1, 21
	v_writelane_b32 v255, s4, 22
	v_writelane_b32 v255, s5, 23
	v_writelane_b32 v255, s6, 24
	v_writelane_b32 v255, s7, 25
	v_writelane_b32 v255, s8, 26
	v_writelane_b32 v255, s9, 27
	v_writelane_b32 v255, s12, 28
	v_writelane_b32 v255, s16, 29
	v_writelane_b32 v255, s18, 30
	v_writelane_b32 v255, s19, 31
	v_writelane_b32 v255, s20, 32
	v_writelane_b32 v255, s21, 33
	v_writelane_b32 v255, s23, 34
	v_writelane_b32 v255, s24, 35
	v_writelane_b32 v255, s26, 36
	v_writelane_b32 v255, s34, 37
	v_readlane_b32 s70, v254, 0
	v_readlane_b32 s71, v254, 1
	v_and_b32_e32 v1, 63, v0
	s_mul_i32 s100, s2, 7
	s_nop 3
	s_sub_u32 s70, s70, 0xc0
	s_subb_u32 s71, s71, 0
	s_add_u32 s101, s101, s100
	s_sub_u32 s101, s101, 1
	s_mov_b32 s100, 224
	s_mov_b32 s0, 0x700
	v_writelane_b32 v255, s0, 2
	s_mov_b32 s0, 0x4400
	v_writelane_b32 v255, s0, 3
	s_mov_b32 s98, 4
	s_mov_b32 s99, 1
	s_mov_b64 s[4:5], -1
	s_branch .Lp4_conv_entry

; __device__ __forceinline__ unsigned xb_ld(unsigned* p)              { return __hip_atomic_load(p, __ATOMIC_RELAXED, __HIP_MEMORY_SCOPE_AGENT); }
; __device__ __forceinline__ unsigned xb_add(unsigned* p, unsigned v) { return __hip_atomic_fetch_add(p, v, __ATOMIC_RELAXED, __HIP_MEMORY_SCOPE_AGENT); }
; #define XB_SPIN(cond, bar) do { unsigned _sp = 0; while (cond) { __builtin_amdgcn_s_sleep(1); \
;     if ((++_sp & 255u) == 0u) { if (xb_ld(&(bar)[XB_TMO])) break; if (_sp > XB_SPIN_CAP) { atomicAdd(&(bar)[XB_TMO], 1u); break; } } } } while (0)
; #define SEAM(k) do { if (IN(k) && IN((k) + 1)) xcd_barrier(bar); } while (0)
; __device__ __forceinline__ void xcd_barrier(const XcdBarrier& b) {
;     asm volatile("s_waitcnt vmcnt(0)" ::: "memory");
;     __syncthreads();
;     if (threadIdx.x == 0) {
;         unsigned* bar = b.bar;
;         __builtin_amdgcn_s_waitcnt(0);
;         unsigned nloc = b.st[0], nx = b.st[1];
;         if (nloc == 0u) { xcd_barrier_complete(bar, b.x, nloc, nx); b.st[0] = nloc; b.st[1] = nx; }
;         const unsigned old = xb_add(&bar[XB_XSUB(b.x)], 1u);
;         const unsigned gen = old / nloc;
;         if (old + 1u == (gen + 1u) * nloc) {
;             __builtin_amdgcn_fence(__ATOMIC_RELEASE, "agent");
;             asm volatile("s_waitcnt vmcnt(0)" ::: "memory");
;             const unsigned og = xb_add(&bar[XB_TOP], 1u);
;             const unsigned tg = og / nx;
;             if (og + 1u == (tg + 1u) * nx) xb_add(&bar[XB_TOPGEN], 1u);
;             else XB_SPIN(xb_ld(&bar[XB_TOPGEN]) == tg, bar);
;             __builtin_amdgcn_fence(__ATOMIC_ACQUIRE, "agent");
;             xb_add(&bar[XB_XGEN(b.x)], 1u);
;             asm volatile("s_waitcnt vmcnt(0)" ::: "memory");
;         } else {
;             XB_SPIN(xb_ld(&bar[XB_XGEN(b.x)]) == gen, bar);
;             __builtin_amdgcn_fence(__ATOMIC_ACQUIRE, "agent");
;             asm volatile("s_waitcnt vmcnt(0)" ::: "memory");
;         }
;     }
;     __syncthreads();
; }
; __global__ void __launch_bounds__(NWAVES * 64, 2) mk_fwd(Args args) {
;     ...
;     SEAM(5);
;     if (IN(6)) {
.LBB0_881:
	s_or_b64 exec, exec, s[4:5]
	s_cmp_lg_u32 s80, 0x100
	s_cbranch_scc1 .Lsh_skip_5
	s_cmp_lg_u32 s74, 0
	s_cbranch_scc1 .Lsh_skip_5
	s_cmp_lg_u32 s75, 12
	s_cbranch_scc1 .Lsh_skip_5
	v_readfirstlane_b32 s101, v0
	s_nop 3
	s_lshr_b32 s101, s101, 6
	s_cmp_eq_u32 s101, 0
	s_cbranch_scc1 .Lsh_skip_5
	s_sleep 100
	v_writelane_b32 v255, s0, 20
	v_writelane_b32 v255, s1, 21
	v_writelane_b32 v255, s4, 22
	v_writelane_b32 v255, s5, 23
	v_writelane_b32 v255, s6, 24
	v_writelane_b32 v255, s7, 25
	v_writelane_b32 v255, s8, 26
	v_writelane_b32 v255, s9, 27
	v_writelane_b32 v255, s12, 28
	v_writelane_b32 v255, s16, 29
	v_writelane_b32 v255, s18, 30
	v_writelane_b32 v255, s19, 31
	v_writelane_b32 v255, s20, 32
	v_writelane_b32 v255, s21, 33
	v_writelane_b32 v255, s23, 34
	v_writelane_b32 v255, s24, 35
	v_writelane_b32 v255, s26, 36
	v_writelane_b32 v255, s34, 37
	v_readlane_b32 s70, v254, 0
	v_readlane_b32 s71, v254, 1
	v_and_b32_e32 v1, 63, v0
	s_mul_i32 s100, s2, 7
	s_nop 3
	s_sub_u32 s70, s70, 0xc0
	s_subb_u32 s71, s71, 0
	s_add_u32 s101, s101, s100
	s_sub_u32 s101, s101, 1
	s_mov_b32 s100, 224
	s_mov_b32 s0, 0x700
	v_writelane_b32 v255, s0, 2
	s_mov_b32 s0, 0x4b00
	v_writelane_b32 v255, s0, 3
	s_mov_b32 s98, 5
	s_mov_b32 s99, 1
	s_mov_b64 s[4:5], -1
	s_branch .Lp4_conv_entry

; __device__ __forceinline__ unsigned xb_ld(unsigned* p)              { return __hip_atomic_load(p, __ATOMIC_RELAXED, __HIP_MEMORY_SCOPE_AGENT); }
; __device__ __forceinline__ unsigned xb_add(unsigned* p, unsigned v) { return __hip_atomic_fetch_add(p, v, __ATOMIC_RELAXED, __HIP_MEMORY_SCOPE_AGENT); }
; #define XB_SPIN(cond, bar) do { unsigned _sp = 0; while (cond) { __builtin_amdgcn_s_sleep(1); \
;     if ((++_sp & 255u) == 0u) { if (xb_ld(&(bar)[XB_TMO])) break; if (_sp > XB_SPIN_CAP) { atomicAdd(&(bar)[XB_TMO], 1u); break; } } } } while (0)
; #define SEAM(k) do { if (IN(k) && IN((k) + 1)) xcd_barrier(bar); } while (0)
; __device__ __forceinline__ void xcd_barrier(const XcdBarrier& b) {
;     asm volatile("s_waitcnt vmcnt(0)" ::: "memory");
;     __syncthreads();
;     if (threadIdx.x == 0) {
;         unsigned* bar = b.bar;
;         __builtin_amdgcn_s_waitcnt(0);
;         unsigned nloc = b.st[0], nx = b.st[1];
;         if (nloc == 0u) { xcd_barrier_complete(bar, b.x, nloc, nx); b.st[0] = nloc; b.st[1] = nx; }
;         const unsigned old = xb_add(&bar[XB_XSUB(b.x)], 1u);
;         const unsigned gen = old / nloc;
;         if (old + 1u == (gen + 1u) * nloc) {
;             __builtin_amdgcn_fence(__ATOMIC_RELEASE, "agent");
;             asm volatile("s_waitcnt vmcnt(0)" ::: "memory");
;             const unsigned og = xb_add(&bar[XB_TOP], 1u);
;             const unsigned tg = og / nx;
;             if (og + 1u == (tg + 1u) * nx) xb_add(&bar[XB_TOPGEN], 1u);
;             else XB_SPIN(xb_ld(&bar[XB_TOPGEN]) == tg, bar);
;             __builtin_amdgcn_fence(__ATOMIC_ACQUIRE, "agent");
;             xb_add(&bar[XB_XGEN(b.x)], 1u);
;             asm volatile("s_waitcnt vmcnt(0)" ::: "memory");
;         } else {
;             XB_SPIN(xb_ld(&bar[XB_XGEN(b.x)]) == gen, bar);
;             __builtin_amdgcn_fence(__ATOMIC_ACQUIRE, "agent");
;             asm volatile("s_waitcnt vmcnt(0)" ::: "memory");
;         }
;     }
;     __syncthreads();
; }
; __global__ void __launch_bounds__(NWAVES * 64, 2) mk_fwd(Args args) {
;     ...
;     SEAM(6);
;     if (IN(7)) { for (int u = bx; u < 256; u += G) cross_unit(lds, (const float*)(ws + WS_CQ), (const float*)(ws + WS_CKV), P.cq_norm, P.ck_norm, (bf16*)(ws + WS_CO), u, tid); __syncthreads(); }
.LBB0_978:
	s_or_b64 exec, exec, s[4:5]
	s_cmp_lg_u32 s80, 0x100
	s_cbranch_scc1 .Lsh_skip_6
	s_cmp_lg_u32 s74, 0
	s_cbranch_scc1 .Lsh_skip_6
	s_cmp_lg_u32 s75, 12
	s_cbranch_scc1 .Lsh_skip_6
	v_readfirstlane_b32 s101, v0
	s_nop 3
	s_lshr_b32 s101, s101, 6
	s_cmp_eq_u32 s101, 0
	s_cbranch_scc1 .Lsh_skip_6
	s_sleep 100
	v_writelane_b32 v255, s0, 20
	v_writelane_b32 v255, s1, 21
	v_writelane_b32 v255, s4, 22
	v_writelane_b32 v255, s5, 23
	v_writelane_b32 v255, s6, 24
	v_writelane_b32 v255, s7, 25
	v_writelane_b32 v255, s8, 26
	v_writelane_b32 v255, s9, 27
	v_writelane_b32 v255, s12, 28
	v_writelane_b32 v255, s16, 29
	v_writelane_b32 v255, s18, 30
	v_writelane_b32 v255, s19, 31
	v_writelane_b32 v255, s20, 32
	v_writelane_b32 v255, s21, 33
	v_writelane_b32 v255, s23, 34
	v_writelane_b32 v255, s24, 35
	v_writelane_b32 v255, s26, 36
	v_writelane_b32 v255, s34, 37
	v_readlane_b32 s70, v254, 0
	v_readlane_b32 s71, v254, 1
	v_and_b32_e32 v1, 63, v0
	s_mul_i32 s100, s2, 7
	s_nop 3
	s_sub_u32 s70, s70, 0xc0
	s_subb_u32 s71, s71, 0
	s_add_u32 s101, s101, s100
	s_sub_u32 s101, s101, 1
	s_mov_b32 s100, 224
	s_mov_b32 s0, 0x700
	v_writelane_b32 v255, s0, 2
	s_mov_b32 s0, 0x5200
	v_writelane_b32 v255, s0, 3
	s_mov_b32 s98, 6
	s_mov_b32 s99, 1
	s_mov_b64 s[4:5], -1
	s_branch .Lp4_conv_entry

; __device__ __forceinline__ unsigned xb_ld(unsigned* p)              { return __hip_atomic_load(p, __ATOMIC_RELAXED, __HIP_MEMORY_SCOPE_AGENT); }
; __device__ __forceinline__ unsigned xb_add(unsigned* p, unsigned v) { return __hip_atomic_fetch_add(p, v, __ATOMIC_RELAXED, __HIP_MEMORY_SCOPE_AGENT); }
; #define XB_SPIN(cond, bar) do { unsigned _sp = 0; while (cond) { __builtin_amdgcn_s_sleep(1); \
;     if ((++_sp & 255u) == 0u) { if (xb_ld(&(bar)[XB_TMO])) break; if (_sp > XB_SPIN_CAP) { atomicAdd(&(bar)[XB_TMO], 1u); break; } } } } while (0)
; #define SEAM(k) do { if (IN(k) && IN((k) + 1)) xcd_barrier(bar); } while (0)
; __device__ __forceinline__ void xcd_barrier(const XcdBarrier& b) {
;     asm volatile("s_waitcnt vmcnt(0)" ::: "memory");
;     __syncthreads();
;     if (threadIdx.x == 0) {
;         unsigned* bar = b.bar;
;         __builtin_amdgcn_s_waitcnt(0);
;         unsigned nloc = b.st[0], nx = b.st[1];
;         if (nloc == 0u) { xcd_barrier_complete(bar, b.x, nloc, nx); b.st[0] = nloc; b.st[1] = nx; }
;         const unsigned old = xb_add(&bar[XB_XSUB(b.x)], 1u);
;         const unsigned gen = old / nloc;
;         if (old + 1u == (gen + 1u) * nloc) {
;             __builtin_amdgcn_fence(__ATOMIC_RELEASE, "agent");
;             asm volatile("s_waitcnt vmcnt(0)" ::: "memory");
;             const unsigned og = xb_add(&bar[XB_TOP], 1u);
;             const unsigned tg = og / nx;
;             if (og + 1u == (tg + 1u) * nx) xb_add(&bar[XB_TOPGEN], 1u);
;             else XB_SPIN(xb_ld(&bar[XB_TOPGEN]) == tg, bar);
;             __builtin_amdgcn_fence(__ATOMIC_ACQUIRE, "agent");
;             xb_add(&bar[XB_XGEN(b.x)], 1u);
;             asm volatile("s_waitcnt vmcnt(0)" ::: "memory");
;         } else {
;             XB_SPIN(xb_ld(&bar[XB_XGEN(b.x)]) == gen, bar);
;             __builtin_amdgcn_fence(__ATOMIC_ACQUIRE, "agent");
;             asm volatile("s_waitcnt vmcnt(0)" ::: "memory");
;         }
;     }
;     __syncthreads();
; }
; __global__ void __launch_bounds__(NWAVES * 64, 2) mk_fwd(Args args) {
;     ...
;     SEAM(7);
;     if (IN(8)) {
.LBB0_1055:
	s_or_b64 exec, exec, s[4:5]
	s_cmp_lg_u32 s80, 0x100
	s_cbranch_scc1 .Lsh_skip_7
	s_cmp_lg_u32 s74, 0
	s_cbranch_scc1 .Lsh_skip_7
	s_cmp_lg_u32 s75, 12
	s_cbranch_scc1 .Lsh_skip_7
	v_readfirstlane_b32 s101, v0
	s_nop 3
	s_lshr_b32 s101, s101, 6
	s_cmp_eq_u32 s101, 0
	s_cbranch_scc1 .Lsh_skip_7
	s_sleep 100
	v_writelane_b32 v255, s0, 20
	v_writelane_b32 v255, s1, 21
	v_writelane_b32 v255, s4, 22
	v_writelane_b32 v255, s5, 23
	v_writelane_b32 v255, s6, 24
	v_writelane_b32 v255, s7, 25
	v_writelane_b32 v255, s8, 26
	v_writelane_b32 v255, s9, 27
	v_writelane_b32 v255, s12, 28
	v_writelane_b32 v255, s16, 29
	v_writelane_b32 v255, s18, 30
	v_writelane_b32 v255, s19, 31
	v_writelane_b32 v255, s20, 32
	v_writelane_b32 v255, s21, 33
	v_writelane_b32 v255, s23, 34
	v_writelane_b32 v255, s24, 35
	v_writelane_b32 v255, s26, 36
	v_writelane_b32 v255, s34, 37
	v_readlane_b32 s70, v254, 0
	v_readlane_b32 s71, v254, 1
	v_and_b32_e32 v1, 63, v0
	s_mul_i32 s100, s2, 7
	s_nop 3
	s_sub_u32 s70, s70, 0xc0
	s_subb_u32 s71, s71, 0
	s_add_u32 s101, s101, s100
	s_sub_u32 s101, s101, 1
	s_mov_b32 s100, 224
	s_mov_b32 s0, 0x700
	v_writelane_b32 v255, s0, 2
	s_mov_b32 s0, 0x5900
	v_writelane_b32 v255, s0, 3
	s_mov_b32 s98, 7
	s_mov_b32 s99, 1
	s_mov_b64 s[4:5], -1
	s_branch .Lp4_conv_entry
